# hyena Y-staging loop unrolled 5x with deferred LDS writes so the five global loads overlap instead of serialising
# speedup vs baseline: 1.0433x; 1.0024x over previous
; #define LAS __attribute__((address_space(3)))
; __device__ __forceinline__ void hyena_unit(KP Pk, Frame& F, int l, int cg) {
;     ...
;         const int ci = cs >> (nseq - 1), st = cs & (nseq - 1), ch = cg * 4 + ci, L = st == 0 ? SEQ : LC, nblk = L / 32, pos0 = st == 0 ? 0 : SEQ;
;         __syncthreads();
;         for (int id = F.tid; id < 8 * (L / 8 + 56); id += NTHR) { const int b = id / (L / 8 + 56), c = id % (L / 8 + 56);
;             if (c < L / 8) *(LAS u32x4*)(F.lds + (b * YSTR + HY_PAD + 8 * c) * 2) = *(const u32x4*)(ZT + ((size_t)b * 1536 + 1024 + ch) * KEYS + pos0 + 8 * c);
;             else { const int pc = c - L / 8, off = pc < 28 ? 8 * pc : HY_PAD + L + 8 * (pc - 28); const u32x4 z = {0u, 0u, 0u, 0u};
;                 *(LAS u32x4*)(F.lds + (b * YSTR + off) * 2) = z; *(LAS u32x4*)(F.lds + HY_YB + (b * YSTR + off) * 2) = z; } }
.LBB0_693:
	s_and_b32 s5, s4, s87
	s_cmp_eq_u32 s5, 0
	s_cselect_b32 s75, s0, 0x100
	s_cselect_b32 s34, 0, 0x800
	s_lshr_b32 s5, s75, 3
	s_add_i32 s18, s5, 56
	s_lshl_b32 s19, s18, 3
	v_cmp_le_i32_e32 vcc, s19, v174
	s_waitcnt lgkmcnt(0)
	s_barrier
	s_and_saveexec_b64 s[38:39], vcc
	s_xor_b64 s[38:39], exec, s[38:39]
	s_mov_b32 s35, s61
	s_or_saveexec_b64 s[40:41], s[38:39]
	s_lshr_b32 s37, s4, s87
	s_add_i32 s38, s37, s8
	s_ashr_i32 s39, s38, 31
	v_mov_b64_e32 v[2:3], s[34:35]
	s_xor_b64 exec, exec, s[40:41]
	s_cbranch_execz .LBB0_703
	v_cvt_f32_u32_e32 v1, s18
	s_add_u32 s42, s38, 0x400
	s_addc_u32 s43, s39, 0
	s_lshl_b32 s37, s34, 1
	v_rcp_iflag_f32_e32 v1, v1
	s_add_u32 s44, s16, s37
	s_addc_u32 s45, s17, 0
	s_sub_i32 s37, 0, s18
	v_mul_f32_e32 v1, 0x4f7ffffe, v1
	v_cvt_u32_f32_e32 v1, v1
	s_mov_b32 s35, s61
	s_sub_i32 s74, 0, s19
	s_sub_i32 s85, 0, s75
	v_mul_lo_u32 v2, s37, v1
	v_mul_hi_u32 v2, v1, v2
	v_add_u32_e32 v1, v1, v2
	s_sub_i32 s96, 0, s5
	s_mov_b64 s[46:47], 0
	v_mov_b32_e32 v2, v133
	v_mov_b32_e32 v3, v174
	v_mov_b32_e32 v246, -1
	v_mov_b32_e32 v247, -1
	v_mov_b32_e32 v248, -1
	v_mov_b32_e32 v249, -1
	v_mov_b32_e32 v224, -1
	s_branch .LBB0_698

; #define LAS __attribute__((address_space(3)))
; __device__ __forceinline__ void hyena_unit(KP Pk, Frame& F, int l, int cg) {
;     ...
;         for (int id = F.tid; id < 8 * (L / 8 + 56); id += NTHR) { const int b = id / (L / 8 + 56), c = id % (L / 8 + 56);
;             if (c < L / 8) *(LAS u32x4*)(F.lds + (b * YSTR + HY_PAD + 8 * c) * 2) = *(const u32x4*)(ZT + ((size_t)b * 1536 + 1024 + ch) * KEYS + pos0 + 8 * c);
;             else { const int pc = c - L / 8, off = pc < 28 ? 8 * pc : HY_PAD + L + 8 * (pc - 28); const u32x4 z = {0u, 0u, 0u, 0u};
;                 *(LAS u32x4*)(F.lds + (b * YSTR + off) * 2) = z; *(LAS u32x4*)(F.lds + HY_YB + (b * YSTR + off) * 2) = z; } }
.Lhs0_e:
	s_andn2_saveexec_b64 s[62:63], s[80:81]
	s_cbranch_execz .Lhs0_l
	v_mov_b64_e32 v[8:9], s[42:43]
	s_movk_i32 s60, 0x600
	v_mad_i64_i32 v[8:9], s[80:81], v7, s60, v[8:9]
	v_mov_b64_e32 v[10:11], s[44:45]
	v_mad_u64_u32 v[10:11], s[80:81], v8, s64, v[10:11]
	v_mad_i32_i24 v11, v9, s64, v11
	v_mad_u64_u32 v[8:9], s[80:81], s74, v7, v[2:3]
	v_ashrrev_i32_e32 v9, 31, v8
	v_lshl_add_u64 v[8:9], v[8:9], 1, v[10:11]
	global_load_dwordx4 v[208:211], v[8:9], off
	v_mul_lo_u32 v4, v4, s33
	v_sub_u32_e32 v4, v4, v5
	v_sub_u32_e32 v4, v4, v6
	v_add_u32_e32 v4, v2, v4
	v_lshl_add_u32 v246, v4, 1, 0

; #define LAS __attribute__((address_space(3)))
; __device__ __forceinline__ void hyena_unit(KP Pk, Frame& F, int l, int cg) {
;     ...
;         for (int id = F.tid; id < 8 * (L / 8 + 56); id += NTHR) { const int b = id / (L / 8 + 56), c = id % (L / 8 + 56);
;             if (c < L / 8) *(LAS u32x4*)(F.lds + (b * YSTR + HY_PAD + 8 * c) * 2) = *(const u32x4*)(ZT + ((size_t)b * 1536 + 1024 + ch) * KEYS + pos0 + 8 * c);
;             else { const int pc = c - L / 8, off = pc < 28 ? 8 * pc : HY_PAD + L + 8 * (pc - 28); const u32x4 z = {0u, 0u, 0u, 0u};
;                 *(LAS u32x4*)(F.lds + (b * YSTR + off) * 2) = z; *(LAS u32x4*)(F.lds + HY_YB + (b * YSTR + off) * 2) = z; } }
.Lhs1_e:
	s_andn2_saveexec_b64 s[62:63], s[80:81]
	s_cbranch_execz .Lhs1_l
	v_mov_b64_e32 v[8:9], s[42:43]
	s_movk_i32 s60, 0x600
	v_mad_i64_i32 v[8:9], s[80:81], v7, s60, v[8:9]
	v_mov_b64_e32 v[10:11], s[44:45]
	v_mad_u64_u32 v[10:11], s[80:81], v8, s64, v[10:11]
	v_mad_i32_i24 v11, v9, s64, v11
	v_mad_u64_u32 v[8:9], s[80:81], s74, v7, v[2:3]
	v_ashrrev_i32_e32 v9, 31, v8
	v_lshl_add_u64 v[8:9], v[8:9], 1, v[10:11]
	global_load_dwordx4 v[212:215], v[8:9], off
	v_mul_lo_u32 v4, v4, s33
	v_sub_u32_e32 v4, v4, v5
	v_sub_u32_e32 v4, v4, v6
	v_add_u32_e32 v4, v2, v4
	v_lshl_add_u32 v247, v4, 1, 0

; #define LAS __attribute__((address_space(3)))
; __device__ __forceinline__ void hyena_unit(KP Pk, Frame& F, int l, int cg) {
;     ...
;         for (int id = F.tid; id < 8 * (L / 8 + 56); id += NTHR) { const int b = id / (L / 8 + 56), c = id % (L / 8 + 56);
;             if (c < L / 8) *(LAS u32x4*)(F.lds + (b * YSTR + HY_PAD + 8 * c) * 2) = *(const u32x4*)(ZT + ((size_t)b * 1536 + 1024 + ch) * KEYS + pos0 + 8 * c);
;             else { const int pc = c - L / 8, off = pc < 28 ? 8 * pc : HY_PAD + L + 8 * (pc - 28); const u32x4 z = {0u, 0u, 0u, 0u};
;                 *(LAS u32x4*)(F.lds + (b * YSTR + off) * 2) = z; *(LAS u32x4*)(F.lds + HY_YB + (b * YSTR + off) * 2) = z; } }
.Lhs2_e:
	s_andn2_saveexec_b64 s[62:63], s[80:81]
	s_cbranch_execz .Lhs2_l
	v_mov_b64_e32 v[8:9], s[42:43]
	s_movk_i32 s60, 0x600
	v_mad_i64_i32 v[8:9], s[80:81], v7, s60, v[8:9]
	v_mov_b64_e32 v[10:11], s[44:45]
	v_mad_u64_u32 v[10:11], s[80:81], v8, s64, v[10:11]
	v_mad_i32_i24 v11, v9, s64, v11
	v_mad_u64_u32 v[8:9], s[80:81], s74, v7, v[2:3]
	v_ashrrev_i32_e32 v9, 31, v8
	v_lshl_add_u64 v[8:9], v[8:9], 1, v[10:11]
	global_load_dwordx4 v[216:219], v[8:9], off
	v_mul_lo_u32 v4, v4, s33
	v_sub_u32_e32 v4, v4, v5
	v_sub_u32_e32 v4, v4, v6
	v_add_u32_e32 v4, v2, v4
	v_lshl_add_u32 v248, v4, 1, 0

; #define LAS __attribute__((address_space(3)))
; __device__ __forceinline__ void hyena_unit(KP Pk, Frame& F, int l, int cg) {
;     ...
;         for (int id = F.tid; id < 8 * (L / 8 + 56); id += NTHR) { const int b = id / (L / 8 + 56), c = id % (L / 8 + 56);
;             if (c < L / 8) *(LAS u32x4*)(F.lds + (b * YSTR + HY_PAD + 8 * c) * 2) = *(const u32x4*)(ZT + ((size_t)b * 1536 + 1024 + ch) * KEYS + pos0 + 8 * c);
;             else { const int pc = c - L / 8, off = pc < 28 ? 8 * pc : HY_PAD + L + 8 * (pc - 28); const u32x4 z = {0u, 0u, 0u, 0u};
;                 *(LAS u32x4*)(F.lds + (b * YSTR + off) * 2) = z; *(LAS u32x4*)(F.lds + HY_YB + (b * YSTR + off) * 2) = z; } }
.Lhs3_e:
	s_andn2_saveexec_b64 s[62:63], s[80:81]
	s_cbranch_execz .Lhs3_l
	v_mov_b64_e32 v[8:9], s[42:43]
	s_movk_i32 s60, 0x600
	v_mad_i64_i32 v[8:9], s[80:81], v7, s60, v[8:9]
	v_mov_b64_e32 v[10:11], s[44:45]
	v_mad_u64_u32 v[10:11], s[80:81], v8, s64, v[10:11]
	v_mad_i32_i24 v11, v9, s64, v11
	v_mad_u64_u32 v[8:9], s[80:81], s74, v7, v[2:3]
	v_ashrrev_i32_e32 v9, 31, v8
	v_lshl_add_u64 v[8:9], v[8:9], 1, v[10:11]
	global_load_dwordx4 v[220:223], v[8:9], off
	v_mul_lo_u32 v4, v4, s33
	v_sub_u32_e32 v4, v4, v5
	v_sub_u32_e32 v4, v4, v6
	v_add_u32_e32 v4, v2, v4
	v_lshl_add_u32 v249, v4, 1, 0

; #define LAS __attribute__((address_space(3)))
; __device__ __forceinline__ void hyena_unit(KP Pk, Frame& F, int l, int cg) {
;     ...
;         for (int id = F.tid; id < 8 * (L / 8 + 56); id += NTHR) { const int b = id / (L / 8 + 56), c = id % (L / 8 + 56);
;             if (c < L / 8) *(LAS u32x4*)(F.lds + (b * YSTR + HY_PAD + 8 * c) * 2) = *(const u32x4*)(ZT + ((size_t)b * 1536 + 1024 + ch) * KEYS + pos0 + 8 * c);
;             else { const int pc = c - L / 8, off = pc < 28 ? 8 * pc : HY_PAD + L + 8 * (pc - 28); const u32x4 z = {0u, 0u, 0u, 0u};
;                 *(LAS u32x4*)(F.lds + (b * YSTR + off) * 2) = z; *(LAS u32x4*)(F.lds + HY_YB + (b * YSTR + off) * 2) = z; } }
.Lhs4_e:
	s_andn2_saveexec_b64 s[62:63], s[80:81]
	s_cbranch_execz .Lhs4_l
	v_mov_b64_e32 v[8:9], s[42:43]
	s_movk_i32 s60, 0x600
	v_mad_i64_i32 v[8:9], s[80:81], v7, s60, v[8:9]
	v_mov_b64_e32 v[10:11], s[44:45]
	v_mad_u64_u32 v[10:11], s[80:81], v8, s64, v[10:11]
	v_mad_i32_i24 v11, v9, s64, v11
	v_mad_u64_u32 v[8:9], s[80:81], s74, v7, v[2:3]
	v_ashrrev_i32_e32 v9, 31, v8
	v_lshl_add_u64 v[8:9], v[8:9], 1, v[10:11]
	global_load_dwordx4 v[242:245], v[8:9], off
	v_mul_lo_u32 v4, v4, s33
	v_sub_u32_e32 v4, v4, v5
	v_sub_u32_e32 v4, v4, v6
	v_add_u32_e32 v4, v2, v4
	v_lshl_add_u32 v224, v4, 1, 0

; #define LAS __attribute__((address_space(3)))
; __device__ __forceinline__ void hyena_unit(KP Pk, Frame& F, int l, int cg) {
;     ...
;         for (int id = F.tid; id < 8 * (L / 8 + 56); id += NTHR) { const int b = id / (L / 8 + 56), c = id % (L / 8 + 56);
;             if (c < L / 8) *(LAS u32x4*)(F.lds + (b * YSTR + HY_PAD + 8 * c) * 2) = *(const u32x4*)(ZT + ((size_t)b * 1536 + 1024 + ch) * KEYS + pos0 + 8 * c);
;             else { const int pc = c - L / 8, off = pc < 28 ? 8 * pc : HY_PAD + L + 8 * (pc - 28); const u32x4 z = {0u, 0u, 0u, 0u};
;                 *(LAS u32x4*)(F.lds + (b * YSTR + off) * 2) = z; *(LAS u32x4*)(F.lds + HY_YB + (b * YSTR + off) * 2) = z; } }
.LBB0_702:
	s_or_b64 exec, exec, s[46:47]
	s_waitcnt vmcnt(0)
	v_cmp_ne_u32_e32 vcc, -1, v246
	s_and_saveexec_b64 s[62:63], vcc
	ds_write_b128 v246, v[208:211] offset:448
	s_or_b64 exec, exec, s[62:63]
	v_cmp_ne_u32_e32 vcc, -1, v247
	s_and_saveexec_b64 s[62:63], vcc
	ds_write_b128 v247, v[212:215] offset:448
	s_or_b64 exec, exec, s[62:63]
	v_cmp_ne_u32_e32 vcc, -1, v248
	s_and_saveexec_b64 s[62:63], vcc
	ds_write_b128 v248, v[216:219] offset:448
	s_or_b64 exec, exec, s[62:63]
	v_cmp_ne_u32_e32 vcc, -1, v249
	s_and_saveexec_b64 s[62:63], vcc
	ds_write_b128 v249, v[220:223] offset:448
	s_or_b64 exec, exec, s[62:63]
	v_cmp_ne_u32_e32 vcc, -1, v224
	s_and_saveexec_b64 s[62:63], vcc
	ds_write_b128 v224, v[242:245] offset:448
	s_or_b64 exec, exec, s[62:63]
	v_mov_b64_e32 v[2:3], s[34:35]
